# plus final-kernel 64 loads in flight; layer-0 projector enc loads 8-deep; layer-1 projector step order interleaves cross-direction items across both projector waves
# speedup vs baseline: 1.0549x; 1.0549x over previous
.LBB0_13:
	v_add_u32_e32 v70, 2, v70
	v_cndmask_b32_e64 v66, v71, v70, s[6:7]
	v_lshl_or_b32 v66, v66, 13, v75
	v_lshl_add_u64 v[80:81], v[68:69], 0, v[66:67]
	global_load_dwordx4 v[76:79], v[80:81], off
	global_load_dwordx4 v[86:89], v[80:81], off offset:64
	global_load_dwordx4 v[94:97], v[80:81], off offset:128
	global_load_dwordx4 v[98:101], v[80:81], off offset:192
	global_load_dwordx4 v[102:105], v[80:81], off offset:256
	global_load_dwordx4 v[106:109], v[80:81], off offset:320
	global_load_dwordx4 v[110:113], v[80:81], off offset:384
	global_load_dwordx4 v[114:117], v[80:81], off offset:448
	v_cmp_lt_u32_e32 vcc, 27, v70
	v_add_u32_e32 v71, -2, v71
	s_or_b64 s[28:29], vcc, s[28:29]
	s_waitcnt vmcnt(7)
	v_mfma_f32_16x16x32_f16 a[8:11], v[2:5], v[76:79], a[0:3]
	v_mfma_f32_16x16x32_f16 a[12:15], v[30:33], v[76:79], a[4:7]
	s_waitcnt vmcnt(6)
	v_mfma_f32_16x16x32_f16 a[8:11], v[6:9], v[86:89], a[8:11]
	v_mfma_f32_16x16x32_f16 a[12:15], v[34:37], v[86:89], a[12:15]
	s_waitcnt vmcnt(5)
	v_mfma_f32_16x16x32_f16 a[8:11], v[10:13], v[94:97], a[8:11]
	v_mfma_f32_16x16x32_f16 a[12:15], v[38:41], v[94:97], a[12:15]
	s_waitcnt vmcnt(4)
	v_mfma_f32_16x16x32_f16 a[8:11], v[14:17], v[98:101], a[8:11]
	v_mfma_f32_16x16x32_f16 a[12:15], v[42:45], v[98:101], a[12:15]
	s_waitcnt vmcnt(3)
	v_mfma_f32_16x16x32_f16 a[8:11], v[26:29], v[102:105], a[8:11]
	v_mfma_f32_16x16x32_f16 a[12:15], v[50:53], v[102:105], a[12:15]
	s_waitcnt vmcnt(2)
	v_mfma_f32_16x16x32_f16 a[8:11], v[18:21], v[106:109], a[8:11]
	v_mfma_f32_16x16x32_f16 a[12:15], v[54:57], v[106:109], a[12:15]
	s_waitcnt vmcnt(1)
	v_mfma_f32_16x16x32_f16 a[8:11], v[22:25], v[110:113], a[8:11]
	v_mfma_f32_16x16x32_f16 a[12:15], v[58:61], v[110:113], a[12:15]
	s_waitcnt vmcnt(0)
	v_mfma_f32_16x16x32_f16 a[8:11], v[46:49], v[114:117], a[8:11]
	v_mfma_f32_16x16x32_f16 a[12:15], v[62:65], v[114:117], a[12:15]
	s_nop 6
	ds_write_b128 v73, a[8:11]
	ds_write_b128 v73, a[12:15] offset:1024
	v_add_u32_e32 v73, 0x1000, v73
	ds_write_b32 v72, v74
	v_add_u32_e32 v72, 8, v72
	s_andn2_b64 exec, exec, s[28:29]
	s_cbranch_execnz .LBB0_13
	s_or_b64 exec, exec, s[28:29]
	s_lshl_b64 s[4:5], s[4:5], 15
	s_add_u32 s4, s40, s4
	s_addc_u32 s5, s41, s5
	v_lshlrev_b32_e32 v194, 4, v130
	v_mov_b32_e32 v195, 0
	v_lshl_add_u64 v[110:111], s[4:5], 0, v[194:195]
	global_load_dwordx4 v[2:5], v194, s[4:5]
	global_load_dwordx4 v[6:9], v194, s[4:5] offset:1024
	global_load_dwordx4 v[10:13], v194, s[4:5] offset:2048
	global_load_dwordx4 v[14:17], v194, s[4:5] offset:3072
	s_movk_i32 s4, 0x1000
	v_add_co_u32_e32 v86, vcc, s4, v110
	s_movk_i32 s4, 0x2000
	s_nop 0
	v_addc_co_u32_e32 v87, vcc, 0, v111, vcc
	v_add_co_u32_e32 v88, vcc, s4, v110
	s_movk_i32 s4, 0x3000
	s_nop 0
	v_addc_co_u32_e32 v89, vcc, 0, v111, vcc
	v_add_co_u32_e32 v90, vcc, s4, v110
	s_movk_i32 s4, 0x4000
	s_nop 0
	v_addc_co_u32_e32 v91, vcc, 0, v111, vcc
	v_add_co_u32_e32 v92, vcc, s4, v110
	s_movk_i32 s4, 0x5000
	s_nop 0
	v_addc_co_u32_e32 v93, vcc, 0, v111, vcc
	s_lshl_b32 s28, s30, 2
	v_add_co_u32_e32 v112, vcc, s4, v110
	s_add_u32 s4, s48, s28
	s_addc_u32 s5, s49, 0
	global_load_dwordx4 v[18:21], v[86:87], off offset:1024
	global_load_dwordx4 v[22:25], v[86:87], off offset:2048
	global_load_dwordx4 v[26:29], v[88:89], off offset:-4096
	global_load_dwordx4 v[30:33], v[88:89], off
	global_load_dwordx4 v[34:37], v[88:89], off offset:1024
	global_load_dwordx4 v[38:41], v[88:89], off offset:2048
	global_load_dwordx4 v[42:45], v[88:89], off offset:3072
	global_load_dwordx4 v[46:49], v[92:93], off offset:-4096
	global_load_dwordx4 v[50:53], v[86:87], off offset:3072
	global_load_dwordx4 v[54:57], v[90:91], off offset:1024
	global_load_dwordx4 v[58:61], v[90:91], off offset:2048
	global_load_dwordx4 v[62:65], v[90:91], off offset:3072
	global_load_dwordx4 v[66:69], v[92:93], off
	global_load_dwordx4 v[70:73], v[92:93], off offset:1024
	global_load_dwordx4 v[74:77], v[92:93], off offset:2048
	global_load_dwordx4 v[78:81], v[92:93], off offset:3072
	v_lshl_add_u64 v[86:87], s[4:5], 0, v[82:83]
	s_add_u32 s4, s50, s28
	s_addc_u32 s5, s51, 0
	v_addc_co_u32_e32 v113, vcc, 0, v111, vcc
	v_lshl_add_u64 v[82:83], s[4:5], 0, v[82:83]
	s_movk_i32 s4, 0x6000
	v_lshlrev_b32_e32 v194, 2, v84
	v_add_co_u32_e32 v106, vcc, s4, v110
	v_lshl_add_u64 v[84:85], v[86:87], 0, v[194:195]
	v_lshl_add_u64 v[82:83], v[82:83], 0, v[194:195]
	v_addc_co_u32_e32 v107, vcc, 0, v111, vcc
	s_movk_i32 s4, 0x7000
	global_load_dwordx4 v[138:141], v[84:85], off
	global_load_dwordx4 v[142:145], v[82:83], off
	global_load_dwordx4 v[146:149], v[84:85], off offset:2048
	global_load_dwordx4 v[150:153], v[82:83], off offset:2048
	s_nop 0
	global_load_dwordx4 v[82:85], v[112:113], off offset:1024
	global_load_dwordx4 v[86:89], v[112:113], off offset:2048
	global_load_dwordx4 v[90:93], v[106:107], off offset:-4096
	global_load_dwordx4 v[94:97], v[106:107], off
	global_load_dwordx4 v[98:101], v[106:107], off offset:1024
	global_load_dwordx4 v[102:105], v[106:107], off offset:2048
	s_nop 0
	global_load_dwordx4 v[106:109], v[106:107], off offset:3072
	v_add_co_u32_e32 v126, vcc, s4, v110
	s_mov_b32 s4, 0xbfb8aa3b
	s_nop 0
	v_addc_co_u32_e32 v127, vcc, 0, v111, vcc
	global_load_dwordx4 v[110:113], v[112:113], off offset:3072
	s_nop 0
	global_load_dwordx4 v[114:117], v[126:127], off
	global_load_dwordx4 v[118:121], v[126:127], off offset:1024
	global_load_dwordx4 v[122:125], v[126:127], off offset:2048
	s_nop 0
	global_load_dwordx4 v[126:129], v[126:127], off offset:3072
	v_add_u32_e32 v204, -1, v1
	v_lshl_add_u32 v1, v130, 4, 0
	v_and_b32_e32 v130, 0x78, v131
	v_lshl_or_b32 v205, v136, 7, v130
	v_or_b32_e32 v206, 0x1e000, v205
	s_mov_b64 s[28:29], 0
	s_mov_b64 s[30:31], 0x1000
	s_mov_b32 s40, 0xfffeffff
	v_mov_b32_e32 v207, 2
	s_waitcnt vmcnt(14)
	v_pk_add_f32 v[138:139], v[138:139], v[142:143]
	v_pk_add_f32 v[140:141], v[140:141], v[144:145]
	s_waitcnt vmcnt(12)
	v_pk_add_f32 v[142:143], v[146:147], v[150:151]
	v_pk_mul_f32 v[140:141], v[140:141], s[4:5] op_sel_hi:[1,0]
	v_pk_mul_f32 v[138:139], v[138:139], s[4:5] op_sel_hi:[1,0]
	v_pk_add_f32 v[144:145], v[148:149], v[152:153]
	v_pk_mul_f32 v[132:133], v[132:133], v[142:143]
	s_and_b64 s[4:5], s[6:7], exec
	v_pk_mul_f32 v[134:135], v[134:135], v[144:145]
	s_cselect_b32 s38, -8, -1
	s_cmp_eq_u32 s3, 1
	v_accvgpr_write_b32 a0, v138
	v_accvgpr_write_b32 a4, v132
	s_cselect_b32 s39, -8, -1
	v_cmp_eq_u32_e64 s[4:5], 0, v204
	v_accvgpr_write_b32 a1, v139
	v_accvgpr_write_b32 a2, v140
	v_accvgpr_write_b32 a3, v141
	v_accvgpr_write_b32 a5, v133
	v_accvgpr_write_b32 a6, v134
	v_accvgpr_write_b32 a7, v135
	s_branch .LBB0_16

.LBB0_16:
	v_cmp_gt_u32_e32 vcc, 15, v204
	v_sub_u32_e32 v130, 14, v204
	s_nop 0
	v_cndmask_b32_e32 v208, v204, v130, vcc
	v_sub_u32_e32 v130, 29, v208
	v_cndmask_b32_e64 v130, v130, v208, s[6:7]
	v_lshlrev_b32_e32 v170, 12, v130
	v_or_b32_e32 v130, v170, v205
	v_lshlrev_b32_e32 v194, 1, v130
	v_lshl_add_u64 v[162:163], s[8:9], 0, v[194:195]
	v_lshl_add_u64 v[164:165], s[10:11], 0, v[194:195]
	v_lshl_add_u64 v[166:167], v[162:163], 0, s[30:31]
	v_lshl_add_u64 v[168:169], v[164:165], 0, s[30:31]
	s_mov_b32 s36, 0
	s_branch .LBB0_18

_Z12final_kernelPKfPf:
	s_load_dwordx4 s[4:7], s[0:1], 0x0
	v_mul_u32_u24_e32 v1, 0x19a, v0
	s_movk_i32 s0, 0xa0
	s_mulk_i32 s2, 0xa0
	v_mul_lo_u16_sdwa v2, v1, s0 dst_sel:DWORD dst_unused:UNUSED_PAD src0_sel:WORD_1 src1_sel:DWORD
	s_ashr_i32 s3, s2, 31
	s_mov_b32 s0, 0x199999a
	v_mul_hi_u32 v4, v0, s0
	s_lshl_b64 s[0:1], s[2:3], 2
	v_sub_u16_e32 v6, v0, v2
	s_mov_b32 s3, 0xa0000
	v_mov_b64_e32 v[2:3], s[0:1]
	v_mad_u64_u32 v[4:5], s[0:1], v4, s3, v[2:3]
	v_lshlrev_b32_e32 v2, 2, v6
	v_mov_b32_e32 v3, 0
	v_lshl_add_u64 v[4:5], v[4:5], 0, v[2:3]
	s_waitcnt lgkmcnt(0)
	s_mov_b64 s[8:9], s[4:5]
	global_load_dword v14, v4, s[8:9]
	s_add_u32 s8, s8, 0x2800
	s_addc_u32 s9, s9, 0
	global_load_dword v15, v4, s[8:9]
	s_add_u32 s8, s8, 0x2800
	s_addc_u32 s9, s9, 0
	global_load_dword v16, v4, s[8:9]
	s_add_u32 s8, s8, 0x2800
	s_addc_u32 s9, s9, 0
	global_load_dword v17, v4, s[8:9]
	s_add_u32 s8, s8, 0x2800
	s_addc_u32 s9, s9, 0
	global_load_dword v18, v4, s[8:9]
	s_add_u32 s8, s8, 0x2800
	s_addc_u32 s9, s9, 0
	global_load_dword v19, v4, s[8:9]
	s_add_u32 s8, s8, 0x2800
	s_addc_u32 s9, s9, 0
	global_load_dword v20, v4, s[8:9]
	s_add_u32 s8, s8, 0x2800
	s_addc_u32 s9, s9, 0
	global_load_dword v21, v4, s[8:9]
	s_add_u32 s8, s8, 0x2800
	s_addc_u32 s9, s9, 0
	global_load_dword v22, v4, s[8:9]
	s_add_u32 s8, s8, 0x2800
	s_addc_u32 s9, s9, 0
	global_load_dword v23, v4, s[8:9]
	s_add_u32 s8, s8, 0x2800
	s_addc_u32 s9, s9, 0
	global_load_dword v24, v4, s[8:9]
	s_add_u32 s8, s8, 0x2800
	s_addc_u32 s9, s9, 0
	global_load_dword v25, v4, s[8:9]
	s_add_u32 s8, s8, 0x2800
	s_addc_u32 s9, s9, 0
	global_load_dword v26, v4, s[8:9]
	s_add_u32 s8, s8, 0x2800
	s_addc_u32 s9, s9, 0
	global_load_dword v27, v4, s[8:9]
	s_add_u32 s8, s8, 0x2800
	s_addc_u32 s9, s9, 0
	global_load_dword v28, v4, s[8:9]
	s_add_u32 s8, s8, 0x2800
	s_addc_u32 s9, s9, 0
	global_load_dword v29, v4, s[8:9]
	s_add_u32 s8, s8, 0x2800
	s_addc_u32 s9, s9, 0
	global_load_dword v30, v4, s[8:9]
	s_add_u32 s8, s8, 0x2800
	s_addc_u32 s9, s9, 0
	global_load_dword v31, v4, s[8:9]
	s_add_u32 s8, s8, 0x2800
	s_addc_u32 s9, s9, 0
	global_load_dword v32, v4, s[8:9]
	s_add_u32 s8, s8, 0x2800
	s_addc_u32 s9, s9, 0
	global_load_dword v33, v4, s[8:9]
	s_add_u32 s8, s8, 0x2800
	s_addc_u32 s9, s9, 0
	global_load_dword v34, v4, s[8:9]
	s_add_u32 s8, s8, 0x2800
	s_addc_u32 s9, s9, 0
	global_load_dword v35, v4, s[8:9]
	s_add_u32 s8, s8, 0x2800
	s_addc_u32 s9, s9, 0
	global_load_dword v36, v4, s[8:9]
	s_add_u32 s8, s8, 0x2800
	s_addc_u32 s9, s9, 0
	global_load_dword v37, v4, s[8:9]
	s_add_u32 s8, s8, 0x2800
	s_addc_u32 s9, s9, 0
	global_load_dword v38, v4, s[8:9]
	s_add_u32 s8, s8, 0x2800
	s_addc_u32 s9, s9, 0
	global_load_dword v39, v4, s[8:9]
	s_add_u32 s8, s8, 0x2800
	s_addc_u32 s9, s9, 0
	global_load_dword v40, v4, s[8:9]
	s_add_u32 s8, s8, 0x2800
	s_addc_u32 s9, s9, 0
	global_load_dword v41, v4, s[8:9]
	s_add_u32 s8, s8, 0x2800
	s_addc_u32 s9, s9, 0
	global_load_dword v42, v4, s[8:9]
	s_add_u32 s8, s8, 0x2800
	s_addc_u32 s9, s9, 0
	global_load_dword v43, v4, s[8:9]
	s_add_u32 s8, s8, 0x2800
	s_addc_u32 s9, s9, 0
	global_load_dword v44, v4, s[8:9]
	s_add_u32 s8, s8, 0x2800
	s_addc_u32 s9, s9, 0
	global_load_dword v45, v4, s[8:9]
	s_add_u32 s8, s8, 0x2800
	s_addc_u32 s9, s9, 0
	global_load_dword v46, v4, s[8:9]
	s_add_u32 s8, s8, 0x2800
	s_addc_u32 s9, s9, 0
	global_load_dword v47, v4, s[8:9]
	s_add_u32 s8, s8, 0x2800
	s_addc_u32 s9, s9, 0
	global_load_dword v48, v4, s[8:9]
	s_add_u32 s8, s8, 0x2800
	s_addc_u32 s9, s9, 0
	global_load_dword v49, v4, s[8:9]
	s_add_u32 s8, s8, 0x2800
	s_addc_u32 s9, s9, 0
	global_load_dword v50, v4, s[8:9]
	s_add_u32 s8, s8, 0x2800
	s_addc_u32 s9, s9, 0
	global_load_dword v51, v4, s[8:9]
	s_add_u32 s8, s8, 0x2800
	s_addc_u32 s9, s9, 0
	global_load_dword v52, v4, s[8:9]
	s_add_u32 s8, s8, 0x2800
	s_addc_u32 s9, s9, 0
	global_load_dword v53, v4, s[8:9]
	s_add_u32 s8, s8, 0x2800
	s_addc_u32 s9, s9, 0
	global_load_dword v54, v4, s[8:9]
	s_add_u32 s8, s8, 0x2800
	s_addc_u32 s9, s9, 0
	global_load_dword v55, v4, s[8:9]
	s_add_u32 s8, s8, 0x2800
	s_addc_u32 s9, s9, 0
	global_load_dword v56, v4, s[8:9]
	s_add_u32 s8, s8, 0x2800
	s_addc_u32 s9, s9, 0
	global_load_dword v57, v4, s[8:9]
	s_add_u32 s8, s8, 0x2800
	s_addc_u32 s9, s9, 0
	global_load_dword v58, v4, s[8:9]
	s_add_u32 s8, s8, 0x2800
	s_addc_u32 s9, s9, 0
	global_load_dword v59, v4, s[8:9]
	s_add_u32 s8, s8, 0x2800
	s_addc_u32 s9, s9, 0
	global_load_dword v60, v4, s[8:9]
	s_add_u32 s8, s8, 0x2800
	s_addc_u32 s9, s9, 0
	global_load_dword v61, v4, s[8:9]
	s_add_u32 s8, s8, 0x2800
	s_addc_u32 s9, s9, 0
	global_load_dword v62, v4, s[8:9]
	s_add_u32 s8, s8, 0x2800
	s_addc_u32 s9, s9, 0
	global_load_dword v63, v4, s[8:9]
	s_add_u32 s8, s8, 0x2800
	s_addc_u32 s9, s9, 0
	global_load_dword v64, v4, s[8:9]
	s_add_u32 s8, s8, 0x2800
	s_addc_u32 s9, s9, 0
	global_load_dword v65, v4, s[8:9]
	s_add_u32 s8, s8, 0x2800
	s_addc_u32 s9, s9, 0
	global_load_dword v66, v4, s[8:9]
	s_add_u32 s8, s8, 0x2800
	s_addc_u32 s9, s9, 0
	global_load_dword v67, v4, s[8:9]
	s_add_u32 s8, s8, 0x2800
	s_addc_u32 s9, s9, 0
	global_load_dword v68, v4, s[8:9]
	s_add_u32 s8, s8, 0x2800
	s_addc_u32 s9, s9, 0
	global_load_dword v69, v4, s[8:9]
	s_add_u32 s8, s8, 0x2800
	s_addc_u32 s9, s9, 0
	global_load_dword v70, v4, s[8:9]
	s_add_u32 s8, s8, 0x2800
	s_addc_u32 s9, s9, 0
	global_load_dword v71, v4, s[8:9]
	s_add_u32 s8, s8, 0x2800
	s_addc_u32 s9, s9, 0
	global_load_dword v72, v4, s[8:9]
	s_add_u32 s8, s8, 0x2800
	s_addc_u32 s9, s9, 0
	global_load_dword v73, v4, s[8:9]
	s_add_u32 s8, s8, 0x2800
	s_addc_u32 s9, s9, 0
	global_load_dword v74, v4, s[8:9]
	s_add_u32 s8, s8, 0x2800
	s_addc_u32 s9, s9, 0
	global_load_dword v75, v4, s[8:9]
	s_add_u32 s8, s8, 0x2800
	s_addc_u32 s9, s9, 0
	global_load_dword v76, v4, s[8:9]
	s_add_u32 s8, s8, 0x2800
	s_addc_u32 s9, s9, 0
	global_load_dword v77, v4, s[8:9]
	s_waitcnt vmcnt(63)
	v_add_f32_e32 v3, v3, v14
	s_waitcnt vmcnt(62)
	v_add_f32_e32 v3, v3, v15
	s_waitcnt vmcnt(61)
	v_add_f32_e32 v3, v3, v16
	s_waitcnt vmcnt(60)
	v_add_f32_e32 v3, v3, v17
	s_waitcnt vmcnt(59)
	v_add_f32_e32 v3, v3, v18
	s_waitcnt vmcnt(58)
	v_add_f32_e32 v3, v3, v19
	s_waitcnt vmcnt(57)
	v_add_f32_e32 v3, v3, v20
	s_waitcnt vmcnt(56)
	v_add_f32_e32 v3, v3, v21
	s_waitcnt vmcnt(55)
	v_add_f32_e32 v3, v3, v22
	s_waitcnt vmcnt(54)
	v_add_f32_e32 v3, v3, v23
	s_waitcnt vmcnt(53)
	v_add_f32_e32 v3, v3, v24
	s_waitcnt vmcnt(52)
	v_add_f32_e32 v3, v3, v25
	s_waitcnt vmcnt(51)
	v_add_f32_e32 v3, v3, v26
	s_waitcnt vmcnt(50)
	v_add_f32_e32 v3, v3, v27
	s_waitcnt vmcnt(49)
	v_add_f32_e32 v3, v3, v28
	s_waitcnt vmcnt(48)
	v_add_f32_e32 v3, v3, v29
	s_waitcnt vmcnt(47)
	v_add_f32_e32 v3, v3, v30
	s_waitcnt vmcnt(46)
	v_add_f32_e32 v3, v3, v31
	s_waitcnt vmcnt(45)
	v_add_f32_e32 v3, v3, v32
	s_waitcnt vmcnt(44)
	v_add_f32_e32 v3, v3, v33
	s_waitcnt vmcnt(43)
	v_add_f32_e32 v3, v3, v34
	s_waitcnt vmcnt(42)
	v_add_f32_e32 v3, v3, v35
	s_waitcnt vmcnt(41)
	v_add_f32_e32 v3, v3, v36
	s_waitcnt vmcnt(40)
	v_add_f32_e32 v3, v3, v37
	s_waitcnt vmcnt(39)
	v_add_f32_e32 v3, v3, v38
	s_waitcnt vmcnt(38)
	v_add_f32_e32 v3, v3, v39
	s_waitcnt vmcnt(37)
	v_add_f32_e32 v3, v3, v40
	s_waitcnt vmcnt(36)
	v_add_f32_e32 v3, v3, v41
	s_waitcnt vmcnt(35)
	v_add_f32_e32 v3, v3, v42
	s_waitcnt vmcnt(34)
	v_add_f32_e32 v3, v3, v43
	s_waitcnt vmcnt(33)
	v_add_f32_e32 v3, v3, v44
	s_waitcnt vmcnt(32)
	v_add_f32_e32 v3, v3, v45
	s_waitcnt vmcnt(31)
	v_add_f32_e32 v3, v3, v46
	s_waitcnt vmcnt(30)
	v_add_f32_e32 v3, v3, v47
	s_waitcnt vmcnt(29)
	v_add_f32_e32 v3, v3, v48
	s_waitcnt vmcnt(28)
	v_add_f32_e32 v3, v3, v49
	s_waitcnt vmcnt(27)
	v_add_f32_e32 v3, v3, v50
	s_waitcnt vmcnt(26)
	v_add_f32_e32 v3, v3, v51
	s_waitcnt vmcnt(25)
	v_add_f32_e32 v3, v3, v52
	s_waitcnt vmcnt(24)
	v_add_f32_e32 v3, v3, v53
	s_waitcnt vmcnt(23)
	v_add_f32_e32 v3, v3, v54
	s_waitcnt vmcnt(22)
	v_add_f32_e32 v3, v3, v55
	s_waitcnt vmcnt(21)
	v_add_f32_e32 v3, v3, v56
	s_waitcnt vmcnt(20)
	v_add_f32_e32 v3, v3, v57
	s_waitcnt vmcnt(19)
	v_add_f32_e32 v3, v3, v58
	s_waitcnt vmcnt(18)
	v_add_f32_e32 v3, v3, v59
	s_waitcnt vmcnt(17)
	v_add_f32_e32 v3, v3, v60
	s_waitcnt vmcnt(16)
	v_add_f32_e32 v3, v3, v61
	s_waitcnt vmcnt(15)
	v_add_f32_e32 v3, v3, v62
	s_waitcnt vmcnt(14)
	v_add_f32_e32 v3, v3, v63
	s_waitcnt vmcnt(13)
	v_add_f32_e32 v3, v3, v64
	s_waitcnt vmcnt(12)
	v_add_f32_e32 v3, v3, v65
	s_waitcnt vmcnt(11)
	v_add_f32_e32 v3, v3, v66
	s_waitcnt vmcnt(10)
	v_add_f32_e32 v3, v3, v67
	s_waitcnt vmcnt(9)
	v_add_f32_e32 v3, v3, v68
	s_waitcnt vmcnt(8)
	v_add_f32_e32 v3, v3, v69
	s_waitcnt vmcnt(7)
	v_add_f32_e32 v3, v3, v70
	s_waitcnt vmcnt(6)
	v_add_f32_e32 v3, v3, v71
	s_waitcnt vmcnt(5)
	v_add_f32_e32 v3, v3, v72
	s_waitcnt vmcnt(4)
	v_add_f32_e32 v3, v3, v73
	s_waitcnt vmcnt(3)
	v_add_f32_e32 v3, v3, v74
	s_waitcnt vmcnt(2)
	v_add_f32_e32 v3, v3, v75
	s_waitcnt vmcnt(1)
	v_add_f32_e32 v3, v3, v76
	s_waitcnt vmcnt(0)
	v_add_f32_e32 v3, v3, v77
	s_mov_b32 s0, 0xffff
	v_and_b32_sdwa v1, s0, v1 dst_sel:DWORD dst_unused:UNUSED_PAD src0_sel:DWORD src1_sel:WORD_1
	s_movk_i32 s0, 0x280
	v_mad_u32_u24 v1, v1, s0, v2
	s_movk_i32 s0, 0xa0
	ds_write_b32 v1, v3
	v_cmp_gt_u32_e32 vcc, s0, v0
	v_lshlrev_b32_e32 v1, 2, v0
	s_waitcnt lgkmcnt(0)
	s_barrier
	s_and_saveexec_b64 s[0:1], vcc
	s_cbranch_execz .LBB5_4
	ds_read2_b32 v[2:3], v1 offset1:160
	v_add_u32_e32 v4, 0x400, v1
	ds_read2_b32 v[4:5], v4 offset0:64 offset1:224
	s_waitcnt lgkmcnt(1)
	v_add_f32_e32 v2, v2, v3
	s_waitcnt lgkmcnt(0)
	v_add_f32_e32 v2, v2, v4
	v_add_f32_e32 v2, v2, v5
	v_mul_f32_e32 v2, 0x39800000, v2
	ds_write_b32 v1, v2 offset:2560

	.amdhsa_kernel _Z12final_kernelPKfPf
		.amdhsa_group_segment_fixed_size 3200
		.amdhsa_private_segment_fixed_size 0
		.amdhsa_kernarg_size 16
		.amdhsa_user_sgpr_count 2
		.amdhsa_user_sgpr_dispatch_ptr 0
		.amdhsa_user_sgpr_queue_ptr 0
		.amdhsa_user_sgpr_kernarg_segment_ptr 1
		.amdhsa_user_sgpr_dispatch_id 0
		.amdhsa_user_sgpr_kernarg_preload_length 0
		.amdhsa_user_sgpr_kernarg_preload_offset 0
		.amdhsa_user_sgpr_private_segment_size 0
		.amdhsa_uses_dynamic_stack 0
		.amdhsa_enable_private_segment 0
		.amdhsa_system_sgpr_workgroup_id_x 1
		.amdhsa_system_sgpr_workgroup_id_y 0
		.amdhsa_system_sgpr_workgroup_id_z 0
		.amdhsa_system_sgpr_workgroup_info 0
		.amdhsa_system_vgpr_workitem_id 0
		.amdhsa_next_free_vgpr 78
		.amdhsa_next_free_sgpr 10
		.amdhsa_accum_offset 80
		.amdhsa_reserve_vcc 1
		.amdhsa_float_round_mode_32 0
		.amdhsa_float_round_mode_16_64 0
		.amdhsa_float_denorm_mode_32 3
		.amdhsa_float_denorm_mode_16_64 3
		.amdhsa_dx10_clamp 1
		.amdhsa_ieee_mode 1
		.amdhsa_fp16_overflow 0
		.amdhsa_tg_split 0
		.amdhsa_exception_fp_ieee_invalid_op 0
		.amdhsa_exception_fp_denorm_src 0
		.amdhsa_exception_fp_ieee_div_zero 0
		.amdhsa_exception_fp_ieee_overflow 0
		.amdhsa_exception_fp_ieee_underflow 0
		.amdhsa_exception_fp_ieee_inexact 0
		.amdhsa_exception_int_div_zero 0
	.end_amdhsa_kernel

amdhsa.kernels:
  - .agpr_count:     16
    .args:
      - .address_space:  global
        .offset:         0
        .size:           8
        .value_kind:     global_buffer
      - .address_space:  global
        .offset:         8
        .size:           8
        .value_kind:     global_buffer
      - .address_space:  global
        .offset:         16
        .size:           8
        .value_kind:     global_buffer
      - .address_space:  global
        .offset:         24
        .size:           8
        .value_kind:     global_buffer
      - .address_space:  global
        .offset:         32
        .size:           8
        .value_kind:     global_buffer
      - .address_space:  global
        .offset:         40
        .size:           8
        .value_kind:     global_buffer
      - .address_space:  global
        .offset:         48
        .size:           8
        .value_kind:     global_buffer
      - .address_space:  global
        .offset:         56
        .size:           8
        .value_kind:     global_buffer
      - .address_space:  global
        .offset:         64
        .size:           8
        .value_kind:     global_buffer
      - .address_space:  global
        .offset:         72
        .size:           8
        .value_kind:     global_buffer
      - .address_space:  global
        .offset:         80
        .size:           8
        .value_kind:     global_buffer
      - .address_space:  global
        .offset:         88
        .size:           8
        .value_kind:     global_buffer
      - .address_space:  global
        .offset:         96
        .size:           8
        .value_kind:     global_buffer
      - .address_space:  global
        .offset:         104
        .size:           8
        .value_kind:     global_buffer
      - .address_space:  global
        .offset:         112
        .size:           8
        .value_kind:     global_buffer
      - .address_space:  global
        .offset:         120
        .size:           8
        .value_kind:     global_buffer
      - .address_space:  global
        .offset:         128
        .size:           8
        .value_kind:     global_buffer
      - .address_space:  global
        .offset:         136
        .size:           8
        .value_kind:     global_buffer
      - .address_space:  global
        .offset:         144
        .size:           8
        .value_kind:     global_buffer
      - .address_space:  global
        .offset:         152
        .size:           8
        .value_kind:     global_buffer
    .group_segment_fixed_size: 0
    .kernarg_segment_align: 8
    .kernarg_segment_size: 160
    .language:       OpenCL C
    .language_version:
      - 2
      - 0
    .max_flat_workgroup_size: 256
    .name:           _Z11lstm_kernelPKDF16_PKDv8_DF16_S3_S3_PKfS5_S5_S5_PDF16_S6_PfS5_PS1_PK15HIP_vector_typeIfLj4EES5_S5_S7_S5_S5_S5_
    .private_segment_fixed_size: 0
    .sgpr_count:     70
    .sgpr_spill_count: 0
    .symbol:         _Z11lstm_kernelPKDF16_PKDv8_DF16_S3_S3_PKfS5_S5_S5_PDF16_S6_PfS5_PS1_PK15HIP_vector_typeIfLj4EES5_S5_S7_S5_S5_S5_.kd
    .uniform_work_group_size: 1
    .uses_dynamic_stack: false
    .vgpr_count:     228
    .vgpr_spill_count: 0
    .wavefront_size: 64
  - .agpr_count:     0
    .args:
      - .actual_access:  read_only
        .address_space:  global
        .offset:         0
        .size:           8
        .value_kind:     global_buffer
      - .actual_access:  read_only
        .address_space:  global
        .offset:         8
        .size:           8
        .value_kind:     global_buffer
      - .actual_access:  read_only
        .address_space:  global
        .offset:         16
        .size:           8
        .value_kind:     global_buffer
      - .actual_access:  write_only
        .address_space:  global
        .offset:         24
        .size:           8
        .value_kind:     global_buffer
    .group_segment_fixed_size: 0
    .kernarg_segment_align: 8
    .kernarg_segment_size: 32
    .language:       OpenCL C
    .language_version:
      - 2
      - 0
    .max_flat_workgroup_size: 256
    .name:           _Z12conv1_kernelPKfS0_S0_PDF16_
    .private_segment_fixed_size: 0
    .sgpr_count:     66
    .sgpr_spill_count: 0
    .symbol:         _Z12conv1_kernelPKfS0_S0_PDF16_.kd
    .uniform_work_group_size: 1
    .uses_dynamic_stack: false
    .vgpr_count:     59
    .vgpr_spill_count: 0
    .wavefront_size: 64
  - .agpr_count:     0
    .args:
      - .address_space:  global
        .offset:         0
        .size:           8
        .value_kind:     global_buffer
      - .address_space:  global
        .offset:         8
        .size:           8
        .value_kind:     global_buffer
      - .address_space:  global
        .offset:         16
        .size:           8
        .value_kind:     global_buffer
      - .address_space:  global
        .offset:         24
        .size:           8
        .value_kind:     global_buffer
      - .address_space:  global
        .offset:         32
        .size:           8
        .value_kind:     global_buffer
      - .address_space:  global
        .offset:         40
        .size:           8
        .value_kind:     global_buffer
      - .address_space:  global
        .offset:         48
        .size:           8
        .value_kind:     global_buffer
      - .address_space:  global
        .offset:         56
        .size:           8
        .value_kind:     global_buffer
      - .address_space:  global
        .offset:         64
        .size:           8
        .value_kind:     global_buffer
      - .address_space:  global
        .offset:         72
        .size:           8
        .value_kind:     global_buffer
      - .address_space:  global
        .offset:         80
        .size:           8
        .value_kind:     global_buffer
    .group_segment_fixed_size: 0
    .kernarg_segment_align: 8
    .kernarg_segment_size: 88
    .language:       OpenCL C
    .language_version:
      - 2
      - 0
    .max_flat_workgroup_size: 256
    .name:           _Z11prep_kernelPKfS0_S0_S0_PDv8_DF16_S2_S2_PKiS0_S2_PDv4_j
    .private_segment_fixed_size: 0
    .sgpr_count:     34
    .sgpr_spill_count: 0
    .symbol:         _Z11prep_kernelPKfS0_S0_S0_PDv8_DF16_S2_S2_PKiS0_S2_PDv4_j.kd
    .uniform_work_group_size: 1
    .uses_dynamic_stack: false
    .vgpr_count:     17
    .vgpr_spill_count: 0
    .wavefront_size: 64
  - .agpr_count:     104
    .args:
      - .address_space:  global
        .offset:         0
        .size:           8
        .value_kind:     global_buffer
      - .address_space:  global
        .offset:         8
        .size:           8
        .value_kind:     global_buffer
      - .address_space:  global
        .offset:         16
        .size:           8
        .value_kind:     global_buffer
      - .address_space:  global
        .offset:         24
        .size:           8
        .value_kind:     global_buffer
      - .address_space:  global
        .offset:         32
        .size:           8
        .value_kind:     global_buffer
    .group_segment_fixed_size: 129152
    .kernarg_segment_align: 8
    .kernarg_segment_size: 40
    .language:       OpenCL C
    .language_version:
      - 2
      - 0
    .max_flat_workgroup_size: 256
    .name:           _Z13pconv2_kernelPKDF16_PKDv8_DF16_PKfPfS6_
    .private_segment_fixed_size: 0
    .sgpr_count:     30
    .sgpr_spill_count: 0
    .symbol:         _Z13pconv2_kernelPKDF16_PKDv8_DF16_PKfPfS6_.kd
    .uniform_work_group_size: 1
    .uses_dynamic_stack: false
    .vgpr_count:     324
    .vgpr_spill_count: 0
    .wavefront_size: 64
  - .agpr_count:     40
    .args:
      - .address_space:  global
        .offset:         0
        .size:           8
        .value_kind:     global_buffer
      - .address_space:  global
        .offset:         8
        .size:           8
        .value_kind:     global_buffer
      - .address_space:  global
        .offset:         16
        .size:           8
        .value_kind:     global_buffer
      - .address_space:  global
        .offset:         24
        .size:           8
        .value_kind:     global_buffer
    .group_segment_fixed_size: 41472
    .kernarg_segment_align: 8
    .kernarg_segment_size: 32
    .language:       OpenCL C
    .language_version:
      - 2
      - 0
    .max_flat_workgroup_size: 256
    .name:           _Z11dcap_kernelPKfS0_S0_Pf
    .private_segment_fixed_size: 0
    .sgpr_count:     25
    .sgpr_spill_count: 0
    .symbol:         _Z11dcap_kernelPKfS0_S0_Pf.kd
    .uniform_work_group_size: 1
    .uses_dynamic_stack: false
    .vgpr_count:     244
    .vgpr_spill_count: 0
    .wavefront_size: 64
  - .agpr_count:     0
    .args:
      - .address_space:  global
        .offset:         0
        .size:           8
        .value_kind:     global_buffer
      - .address_space:  global
        .offset:         8
        .size:           8
        .value_kind:     global_buffer
    .group_segment_fixed_size: 3200
    .kernarg_segment_align: 8
    .kernarg_segment_size: 16
    .language:       OpenCL C
    .language_version:
      - 2
      - 0
    .max_flat_workgroup_size: 640
    .name:           _Z12final_kernelPKfPf
    .private_segment_fixed_size: 0
    .sgpr_count:     16
    .sgpr_spill_count: 0
    .symbol:         _Z12final_kernelPKfPf.kd
    .uniform_work_group_size: 1
    .uses_dynamic_stack: false
    .vgpr_count:     78
    .vgpr_spill_count: 0
    .wavefront_size: 64
